# baseline (speedup 1.0000x reference)
.LBB1_8:
	s_or_b64 exec, exec, s[2:3]
	s_mov_b64 s[4:5], s[16:17]
	s_movk_i32 s2, 0x320
	v_cmp_gt_u32_e32 vcc, s2, v0
	s_waitcnt lgkmcnt(0)
	s_barrier
	s_and_saveexec_b64 s[6:7], vcc
	s_cbranch_execz .LBB1_14
	v_and_b32_e32 v3, 7, v0
	v_lshrrev_b32_e32 v1, 3, v0
	v_mul_u32_u24_e32 v4, 0xca0, v3
	v_lshl_add_u32 v8, v1, 2, v4
	ds_read2_b32 v[12:13], v8 offset1:101
	v_lshlrev_b32_e32 v9, 5, v3
	v_add_u32_e32 v4, 0x200, v8
	ds_read2_b32 v[14:15], v4 offset0:74 offset1:175
	v_add_u32_e32 v10, 0x400, v8
	ds_read_b128 v[4:7], v9 offset:25856
	ds_read2_b32 v[16:17], v10 offset0:148 offset1:249
	v_add_u32_e32 v8, 0x800, v8
	ds_read2_b32 v[18:19], v8 offset0:94 offset1:195
	ds_read_b128 v[8:11], v9 offset:25872
	s_movk_i32 s2, 0xff
	s_waitcnt lgkmcnt(3)
	v_cmp_nlt_f32_e32 vcc, v13, v5
	s_nop 1
	v_cndmask_b32_e64 v5, 0, 1, vcc
	v_cmp_nlt_f32_e32 vcc, v12, v4
	v_lshlrev_b16_e32 v5, 1, v5
	s_nop 0
	v_cndmask_b32_e64 v4, 0, 1, vcc
	v_cmp_nlt_f32_e32 vcc, v14, v6
	v_bitop3_b16 v4, v4, 3, v5 bitop3:0xc8
	s_nop 0
	v_cndmask_b32_e64 v5, 0, 1, vcc
	v_cmp_nlt_f32_e32 vcc, v15, v7
	v_lshlrev_b16_e32 v5, 2, v5
	s_nop 0
	v_cndmask_b32_e64 v6, 0, 1, vcc
	v_lshlrev_b16_e32 v6, 3, v6
	v_or_b32_e32 v5, v6, v5
	s_waitcnt lgkmcnt(0)
	v_cmp_nlt_f32_e32 vcc, v18, v10
	v_bitop3_b16 v4, v4, 15, v5 bitop3:0xc8
	s_nop 0
	v_cndmask_b32_e64 v5, 0, 1, vcc
	v_cmp_nlt_f32_e32 vcc, v19, v11
	v_lshlrev_b16_e32 v5, 2, v5
	s_nop 0
	v_cndmask_b32_e64 v6, 0, 1, vcc
	v_lshlrev_b16_e32 v6, 3, v6
	v_cmp_nlt_f32_e32 vcc, v17, v9
	v_or_b32_e32 v5, v6, v5
	s_nop 0
	v_cndmask_b32_e64 v6, 0, 1, vcc
	v_cmp_nlt_f32_e32 vcc, v16, v8
	v_lshlrev_b16_e32 v6, 1, v6
	s_nop 0
	v_cndmask_b32_e64 v7, 0, 1, vcc
	v_or_b32_e32 v6, v7, v6
	v_bitop3_b16 v5, v6, v5, 3 bitop3:0xec
	v_lshlrev_b16_e32 v5, 4, v5
	v_bitop3_b16 v4, v4, s2, v5 bitop3:0xc8
	v_cmp_eq_u16_e32 vcc, 0, v4
	s_nop 1
	v_cndmask_b32_e64 v4, 0, 1, vcc
	s_nop 1
	v_and_b32_dpp v4, v4, v4 quad_perm:[1,0,3,2] row_mask:0xf bank_mask:0xf
	s_nop 1
	v_and_b32_dpp v4, v4, v4 quad_perm:[2,3,0,1] row_mask:0xf bank_mask:0xf
	s_nop 1
	v_and_b32_dpp v4, v4, v4 row_half_mirror row_mask:0xf bank_mask:0xf
	v_cmp_eq_u32_e32 vcc, 0, v3
	v_and_b32_e32 v3, 1, v4
	v_cmp_eq_u32_e64 s[2:3], 1, v3
	s_and_b64 s[2:3], vcc, s[2:3]
	s_and_b64 exec, exec, s[2:3]
	s_cbranch_execz .LBB1_14
	s_mov_b64 s[2:3], exec
	s_brev_b32 s8, -2
